# baseline (speedup 1.0000x reference)
.LBB2_15:
	s_load_dwordx2 s[6:7], s[0:1], 0x30
	s_lshr_b32 s2, s14, 6
	s_mul_i32 s10, s9, 3
	s_mul_i32 s15, s15, 3
	v_lshlrev_b32_e32 v102, 2, v98
	s_lshr_b32 s4, s10, 1
	s_lshl_b32 s2, s2, 4
	v_lshl_or_b32 v103, s8, 6, v1
	s_add_i32 s5, s4, s15
	v_and_or_b32 v1, s2, 16, v102
	s_waitcnt lgkmcnt(0)
	s_barrier
	s_cmp_lt_u32 s5, 32
	v_lshlrev_b32_e32 v98, 3, v1
	v_mov_b32_e32 v99, 0
	s_cselect_b64 s[8:9], -1, 0
	s_cmp_lt_u32 s5, 16
	s_waitcnt lgkmcnt(0)
	v_lshl_add_u64 v[100:101], s[6:7], 0, v[98:99]
	v_or_b32_e32 v98, s12, v103
	s_cselect_b64 s[2:3], -1, 0
	s_cmp_gt_u32 s5, 31
	v_ashrrev_i32_e32 v99, 31, v98
	s_cbranch_scc1 .LBB2_17
	v_lshlrev_b64 v[104:105], 8, v[98:99]
	v_lshl_add_u64 v[108:109], v[100:101], 0, v[104:105]
	global_load_dwordx4 v[104:107], v[108:109], off
	s_nop 0
	global_load_dwordx4 v[108:111], v[108:109], off offset:16
	s_mov_b32 s14, 0x3e38aa3b
	s_waitcnt vmcnt(0)
	v_mov_b32_e32 v113, v106
	v_mov_b32_e32 v106, v105
	v_mov_b32_e32 v105, v110
	v_mov_b32_e32 v110, v109
	v_mov_b32_e32 v112, v104
	v_mov_b32_e32 v104, v108
	v_pk_mul_f32 v[108:109], v[94:95], v[106:107]
	v_pk_mul_f32 v[106:107], v[90:91], v[106:107]
	v_pk_mul_f32 v[114:115], v[96:97], v[110:111]
	v_pk_mul_f32 v[110:111], v[92:93], v[110:111]
	v_pk_fma_f32 v[90:91], v[90:91], v[112:113], v[108:109]
	v_pk_fma_f32 v[94:95], v[94:95], v[112:113], v[106:107] neg_lo:[0,0,1] neg_hi:[0,0,1]
	v_pk_fma_f32 v[92:93], v[92:93], v[104:105], v[114:115]
	v_pk_fma_f32 v[96:97], v[96:97], v[104:105], v[110:111] neg_lo:[0,0,1] neg_hi:[0,0,1]
	s_cmp_lg_u64 s[2:3], 0
	s_cbranch_scc0 .Lqs_skip_0
	v_pk_mul_f32 v[94:95], v[94:95], s[14:15] op_sel_hi:[1,0]
	v_pk_mul_f32 v[96:97], v[96:97], s[14:15] op_sel_hi:[1,0]
	v_pk_mul_f32 v[90:91], v[90:91], s[14:15] op_sel_hi:[1,0]
	v_pk_mul_f32 v[92:93], v[92:93], s[14:15] op_sel_hi:[1,0]
.Lqs_skip_0:
.LBB2_17:
	s_lshl_b32 s4, s4, 7
	s_add_i32 s4, s4, 0
	v_lshl_add_u32 v104, v1, 1, s4
	v_cvt_pk_f16_f32 v97, v96, v97
	v_cvt_pk_f16_f32 v96, v94, v95
	v_cvt_pk_f16_f32 v94, v90, v91
	s_movk_i32 s4, 0x190
	v_or_b32_e32 v90, 16, v103
	v_mul_lo_u32 v1, v103, s4
	v_cndmask_b32_e64 v91, 0, 1, s[8:9]
	v_or_b32_e32 v90, s12, v90
	v_cvt_pk_f16_f32 v95, v92, v93
	v_add_u32_e32 v92, v104, v1
	v_cmp_ne_u32_e64 s[4:5], 1, v91
	s_andn2_b64 vcc, exec, s[8:9]
	v_ashrrev_i32_e32 v91, 31, v90
	ds_write2_b64 v92, v[96:97], v[94:95] offset1:8
	s_cbranch_vccnz .LBB2_19
	v_lshlrev_b64 v[94:95], 8, v[90:91]
	v_lshl_add_u64 v[104:105], v[100:101], 0, v[94:95]
	global_load_dwordx4 v[94:97], v[104:105], off
	s_nop 0
	global_load_dwordx4 v[104:107], v[104:105], off offset:16
	s_mov_b32 s8, 0x3e38aa3b
	s_waitcnt vmcnt(0)
	v_mov_b32_e32 v109, v96
	v_mov_b32_e32 v96, v95
	v_mov_b32_e32 v95, v106
	v_mov_b32_e32 v106, v105
	v_mov_b32_e32 v108, v94
	v_mov_b32_e32 v94, v104
	v_pk_mul_f32 v[104:105], v[86:87], v[96:97]
	v_pk_mul_f32 v[96:97], v[82:83], v[96:97]
	v_pk_mul_f32 v[110:111], v[88:89], v[106:107]
	v_pk_mul_f32 v[106:107], v[84:85], v[106:107]
	v_pk_fma_f32 v[82:83], v[82:83], v[108:109], v[104:105]
	v_pk_fma_f32 v[86:87], v[86:87], v[108:109], v[96:97] neg_lo:[0,0,1] neg_hi:[0,0,1]
	v_pk_fma_f32 v[84:85], v[84:85], v[94:95], v[110:111]
	v_pk_fma_f32 v[88:89], v[88:89], v[94:95], v[106:107] neg_lo:[0,0,1] neg_hi:[0,0,1]
	s_cmp_lg_u64 s[2:3], 0
	s_cbranch_scc0 .Lqs_skip_1
	v_pk_mul_f32 v[86:87], v[86:87], s[8:9] op_sel_hi:[1,0]
	v_pk_mul_f32 v[88:89], v[88:89], s[8:9] op_sel_hi:[1,0]
	v_pk_mul_f32 v[82:83], v[82:83], s[8:9] op_sel_hi:[1,0]
	v_pk_mul_f32 v[84:85], v[84:85], s[8:9] op_sel_hi:[1,0]
.Lqs_skip_1:
.LBB2_19:
	v_cvt_pk_f16_f32 v89, v88, v89
	v_cvt_pk_f16_f32 v88, v86, v87
	v_cvt_pk_f16_f32 v85, v84, v85
	v_cvt_pk_f16_f32 v84, v82, v83
	v_add_u32_e32 v82, 0x1800, v92
	ds_write2_b64 v82, v[88:89], v[84:85] offset0:32 offset1:40
	v_or_b32_e32 v82, 32, v103
	v_or_b32_e32 v82, s12, v82
	s_and_b64 vcc, exec, s[4:5]
	v_ashrrev_i32_e32 v83, 31, v82
	s_cbranch_vccnz .LBB2_21
	v_lshlrev_b64 v[84:85], 8, v[82:83]
	v_lshl_add_u64 v[88:89], v[100:101], 0, v[84:85]
	global_load_dwordx4 v[84:87], v[88:89], off
	global_load_dwordx4 v[94:97], v[88:89], off offset:16
	s_mov_b32 s8, 0x3e38aa3b
	s_waitcnt vmcnt(0)
	v_mov_b32_e32 v89, v86
	v_mov_b32_e32 v86, v85
	v_mov_b32_e32 v85, v96
	v_mov_b32_e32 v96, v95
	v_mov_b32_e32 v88, v84
	v_mov_b32_e32 v84, v94
	v_pk_mul_f32 v[94:95], v[78:79], v[86:87]
	v_pk_mul_f32 v[86:87], v[74:75], v[86:87]
	v_pk_mul_f32 v[104:105], v[80:81], v[96:97]
	v_pk_mul_f32 v[96:97], v[76:77], v[96:97]
	v_pk_fma_f32 v[74:75], v[74:75], v[88:89], v[94:95]
	v_pk_fma_f32 v[78:79], v[78:79], v[88:89], v[86:87] neg_lo:[0,0,1] neg_hi:[0,0,1]
	v_pk_fma_f32 v[76:77], v[76:77], v[84:85], v[104:105]
	v_pk_fma_f32 v[80:81], v[80:81], v[84:85], v[96:97] neg_lo:[0,0,1] neg_hi:[0,0,1]
	s_cmp_lg_u64 s[2:3], 0
	s_cbranch_scc0 .Lqs_skip_2
	v_pk_mul_f32 v[78:79], v[78:79], s[8:9] op_sel_hi:[1,0]
	v_pk_mul_f32 v[80:81], v[80:81], s[8:9] op_sel_hi:[1,0]
	v_pk_mul_f32 v[74:75], v[74:75], s[8:9] op_sel_hi:[1,0]
	v_pk_mul_f32 v[76:77], v[76:77], s[8:9] op_sel_hi:[1,0]
.Lqs_skip_2:
.LBB2_21:
	v_cvt_pk_f16_f32 v81, v80, v81
	v_cvt_pk_f16_f32 v80, v78, v79
	v_cvt_pk_f16_f32 v77, v76, v77
	v_cvt_pk_f16_f32 v76, v74, v75
	v_add_u32_e32 v74, 0x3000, v92
	ds_write2_b64 v74, v[80:81], v[76:77] offset0:64 offset1:72
	v_or_b32_e32 v74, 48, v103
	v_or_b32_e32 v74, s12, v74
	s_and_b64 vcc, exec, s[4:5]
	v_ashrrev_i32_e32 v75, 31, v74
	s_cbranch_vccnz .LBB2_23
	v_lshlrev_b64 v[76:77], 8, v[74:75]
	v_lshl_add_u64 v[80:81], v[100:101], 0, v[76:77]
	global_load_dwordx4 v[76:79], v[80:81], off
	global_load_dwordx4 v[84:87], v[80:81], off offset:16
	s_mov_b32 s4, 0x3e38aa3b
	s_waitcnt vmcnt(0)
	v_mov_b32_e32 v81, v78
	v_mov_b32_e32 v78, v77
	v_mov_b32_e32 v77, v86
	v_mov_b32_e32 v86, v85
	v_mov_b32_e32 v80, v76
	v_mov_b32_e32 v76, v84
	v_pk_mul_f32 v[84:85], v[70:71], v[78:79]
	v_pk_mul_f32 v[78:79], v[66:67], v[78:79]
	v_pk_mul_f32 v[88:89], v[72:73], v[86:87]
	v_pk_mul_f32 v[86:87], v[68:69], v[86:87]
	v_pk_fma_f32 v[66:67], v[66:67], v[80:81], v[84:85]
	v_pk_fma_f32 v[70:71], v[70:71], v[80:81], v[78:79] neg_lo:[0,0,1] neg_hi:[0,0,1]
	v_pk_fma_f32 v[68:69], v[68:69], v[76:77], v[88:89]
	v_pk_fma_f32 v[72:73], v[72:73], v[76:77], v[86:87] neg_lo:[0,0,1] neg_hi:[0,0,1]
	s_cmp_lg_u64 s[2:3], 0
	s_cbranch_scc0 .Lqs_skip_3
	v_pk_mul_f32 v[70:71], v[70:71], s[4:5] op_sel_hi:[1,0]
	v_pk_mul_f32 v[72:73], v[72:73], s[4:5] op_sel_hi:[1,0]
	v_pk_mul_f32 v[66:67], v[66:67], s[4:5] op_sel_hi:[1,0]
	v_pk_mul_f32 v[68:69], v[68:69], s[4:5] op_sel_hi:[1,0]
.Lqs_skip_3:
.LBB2_23:
	s_add_i32 s2, s10, 1
	s_lshr_b32 s4, s2, 1
	v_cvt_pk_f16_f32 v73, v72, v73
	v_cvt_pk_f16_f32 v72, v70, v71
	v_cvt_pk_f16_f32 v69, v68, v69
	v_cvt_pk_f16_f32 v68, v66, v67
	v_add_u32_e32 v66, 0x4800, v92
	s_add_i32 s5, s4, s15
	s_lshl_b32 s2, s2, 4
	ds_write2_b64 v66, v[72:73], v[68:69] offset0:96 offset1:104
	v_and_or_b32 v68, s2, 16, v102
	s_cmp_lt_u32 s5, 32
	s_cselect_b64 s[8:9], -1, 0
	s_cmp_lt_u32 s5, 16
	v_lshlrev_b32_e32 v66, 3, v68
	v_mov_b32_e32 v67, 0
	s_cselect_b64 s[2:3], -1, 0
	s_cmp_gt_u32 s5, 31
	v_lshl_add_u64 v[66:67], s[6:7], 0, v[66:67]
	s_cbranch_scc1 .LBB2_25
	v_lshlrev_b64 v[70:71], 8, v[98:99]
	v_lshl_add_u64 v[76:77], v[66:67], 0, v[70:71]
	global_load_dwordx4 v[70:73], v[76:77], off
	s_nop 0
	global_load_dwordx4 v[76:79], v[76:77], off offset:16
	s_mov_b32 s14, 0x3e38aa3b
	s_waitcnt vmcnt(0)
	v_mov_b32_e32 v81, v72
	v_mov_b32_e32 v72, v71
	v_mov_b32_e32 v71, v78
	v_mov_b32_e32 v78, v77
	v_mov_b32_e32 v80, v70
	v_mov_b32_e32 v70, v76
	v_pk_mul_f32 v[76:77], v[62:63], v[72:73]
	v_pk_mul_f32 v[72:73], v[58:59], v[72:73]
	v_pk_mul_f32 v[84:85], v[64:65], v[78:79]
	v_pk_mul_f32 v[78:79], v[60:61], v[78:79]
	v_pk_fma_f32 v[58:59], v[58:59], v[80:81], v[76:77]
	v_pk_fma_f32 v[62:63], v[62:63], v[80:81], v[72:73] neg_lo:[0,0,1] neg_hi:[0,0,1]
	v_pk_fma_f32 v[60:61], v[60:61], v[70:71], v[84:85]
	v_pk_fma_f32 v[64:65], v[64:65], v[70:71], v[78:79] neg_lo:[0,0,1] neg_hi:[0,0,1]
	s_cmp_lg_u64 s[2:3], 0
	s_cbranch_scc0 .Lqs_skip_4
	v_pk_mul_f32 v[62:63], v[62:63], s[14:15] op_sel_hi:[1,0]
	v_pk_mul_f32 v[64:65], v[64:65], s[14:15] op_sel_hi:[1,0]
	v_pk_mul_f32 v[58:59], v[58:59], s[14:15] op_sel_hi:[1,0]
	v_pk_mul_f32 v[60:61], v[60:61], s[14:15] op_sel_hi:[1,0]
.Lqs_skip_4:
.LBB2_25:
	s_lshl_b32 s4, s4, 7
	s_add_i32 s4, s4, 0
	v_lshl_add_u32 v68, v68, 1, s4
	v_cvt_pk_f16_f32 v61, v60, v61
	v_cvt_pk_f16_f32 v60, v58, v59
	v_cndmask_b32_e64 v59, 0, 1, s[8:9]
	v_cvt_pk_f16_f32 v65, v64, v65
	v_cvt_pk_f16_f32 v64, v62, v63
	v_add_u32_e32 v58, v68, v1
	v_cmp_ne_u32_e64 s[4:5], 1, v59
	s_andn2_b64 vcc, exec, s[8:9]
	ds_write2_b64 v58, v[64:65], v[60:61] offset1:8
	s_cbranch_vccnz .LBB2_27
	v_lshlrev_b64 v[60:61], 8, v[90:91]
	v_lshl_add_u64 v[64:65], v[66:67], 0, v[60:61]
	global_load_dwordx4 v[60:63], v[64:65], off
	global_load_dwordx4 v[68:71], v[64:65], off offset:16
	s_mov_b32 s8, 0x3e38aa3b
	s_waitcnt vmcnt(0)
	v_mov_b32_e32 v65, v62
	v_mov_b32_e32 v62, v61
	v_mov_b32_e32 v61, v70
	v_mov_b32_e32 v70, v69
	v_mov_b32_e32 v64, v60
	v_mov_b32_e32 v60, v68
	v_pk_mul_f32 v[68:69], v[54:55], v[62:63]
	v_pk_mul_f32 v[62:63], v[50:51], v[62:63]
	v_pk_mul_f32 v[72:73], v[56:57], v[70:71]
	v_pk_mul_f32 v[70:71], v[52:53], v[70:71]
	v_pk_fma_f32 v[50:51], v[50:51], v[64:65], v[68:69]
	v_pk_fma_f32 v[54:55], v[54:55], v[64:65], v[62:63] neg_lo:[0,0,1] neg_hi:[0,0,1]
	v_pk_fma_f32 v[52:53], v[52:53], v[60:61], v[72:73]
	v_pk_fma_f32 v[56:57], v[56:57], v[60:61], v[70:71] neg_lo:[0,0,1] neg_hi:[0,0,1]
	s_cmp_lg_u64 s[2:3], 0
	s_cbranch_scc0 .Lqs_skip_5
	v_pk_mul_f32 v[54:55], v[54:55], s[8:9] op_sel_hi:[1,0]
	v_pk_mul_f32 v[56:57], v[56:57], s[8:9] op_sel_hi:[1,0]
	v_pk_mul_f32 v[50:51], v[50:51], s[8:9] op_sel_hi:[1,0]
	v_pk_mul_f32 v[52:53], v[52:53], s[8:9] op_sel_hi:[1,0]
.Lqs_skip_5:
.LBB2_27:
	v_cvt_pk_f16_f32 v57, v56, v57
	v_cvt_pk_f16_f32 v56, v54, v55
	v_cvt_pk_f16_f32 v53, v52, v53
	v_cvt_pk_f16_f32 v52, v50, v51
	v_add_u32_e32 v50, 0x1800, v58
	s_and_b64 vcc, exec, s[4:5]
	ds_write2_b64 v50, v[56:57], v[52:53] offset0:32 offset1:40
	s_cbranch_vccnz .LBB2_29
	v_lshlrev_b64 v[50:51], 8, v[82:83]
	v_lshl_add_u64 v[60:61], v[66:67], 0, v[50:51]
	global_load_dwordx4 v[50:53], v[60:61], off
	global_load_dwordx4 v[54:57], v[60:61], off offset:16
	s_mov_b32 s8, 0x3e38aa3b
	s_waitcnt vmcnt(0)
	v_mov_b32_e32 v61, v52
	v_mov_b32_e32 v52, v51
	v_mov_b32_e32 v51, v56
	v_mov_b32_e32 v56, v55
	v_mov_b32_e32 v60, v50
	v_mov_b32_e32 v50, v54
	v_pk_mul_f32 v[54:55], v[46:47], v[52:53]
	v_pk_mul_f32 v[52:53], v[42:43], v[52:53]
	v_pk_mul_f32 v[62:63], v[48:49], v[56:57]
	v_pk_mul_f32 v[56:57], v[44:45], v[56:57]
	v_pk_fma_f32 v[42:43], v[42:43], v[60:61], v[54:55]
	v_pk_fma_f32 v[46:47], v[46:47], v[60:61], v[52:53] neg_lo:[0,0,1] neg_hi:[0,0,1]
	v_pk_fma_f32 v[44:45], v[44:45], v[50:51], v[62:63]
	v_pk_fma_f32 v[48:49], v[48:49], v[50:51], v[56:57] neg_lo:[0,0,1] neg_hi:[0,0,1]
	s_cmp_lg_u64 s[2:3], 0
	s_cbranch_scc0 .Lqs_skip_6
	v_pk_mul_f32 v[46:47], v[46:47], s[8:9] op_sel_hi:[1,0]
	v_pk_mul_f32 v[48:49], v[48:49], s[8:9] op_sel_hi:[1,0]
	v_pk_mul_f32 v[42:43], v[42:43], s[8:9] op_sel_hi:[1,0]
	v_pk_mul_f32 v[44:45], v[44:45], s[8:9] op_sel_hi:[1,0]
.Lqs_skip_6:
.LBB2_29:
	v_cvt_pk_f16_f32 v49, v48, v49
	v_cvt_pk_f16_f32 v48, v46, v47
	v_cvt_pk_f16_f32 v45, v44, v45
	v_cvt_pk_f16_f32 v44, v42, v43
	v_add_u32_e32 v42, 0x3000, v58
	s_and_b64 vcc, exec, s[4:5]
	ds_write2_b64 v42, v[48:49], v[44:45] offset0:64 offset1:72
	s_cbranch_vccnz .LBB2_31
	v_lshlrev_b64 v[42:43], 8, v[74:75]
	v_lshl_add_u64 v[50:51], v[66:67], 0, v[42:43]
	global_load_dwordx4 v[42:45], v[50:51], off
	global_load_dwordx4 v[46:49], v[50:51], off offset:16
	s_mov_b32 s4, 0x3e38aa3b
	s_waitcnt vmcnt(0)
	v_mov_b32_e32 v51, v44
	v_mov_b32_e32 v44, v43
	v_mov_b32_e32 v43, v48
	v_mov_b32_e32 v48, v47
	v_mov_b32_e32 v50, v42
	v_mov_b32_e32 v42, v46
	v_pk_mul_f32 v[46:47], v[38:39], v[44:45]
	v_pk_mul_f32 v[44:45], v[34:35], v[44:45]
	v_pk_mul_f32 v[52:53], v[40:41], v[48:49]
	v_pk_mul_f32 v[48:49], v[36:37], v[48:49]
	v_pk_fma_f32 v[34:35], v[34:35], v[50:51], v[46:47]
	v_pk_fma_f32 v[38:39], v[38:39], v[50:51], v[44:45] neg_lo:[0,0,1] neg_hi:[0,0,1]
	v_pk_fma_f32 v[36:37], v[36:37], v[42:43], v[52:53]
	v_pk_fma_f32 v[40:41], v[40:41], v[42:43], v[48:49] neg_lo:[0,0,1] neg_hi:[0,0,1]
	s_cmp_lg_u64 s[2:3], 0
	s_cbranch_scc0 .Lqs_skip_7
	v_pk_mul_f32 v[38:39], v[38:39], s[4:5] op_sel_hi:[1,0]
	v_pk_mul_f32 v[40:41], v[40:41], s[4:5] op_sel_hi:[1,0]
	v_pk_mul_f32 v[34:35], v[34:35], s[4:5] op_sel_hi:[1,0]
	v_pk_mul_f32 v[36:37], v[36:37], s[4:5] op_sel_hi:[1,0]
.Lqs_skip_7:
.LBB2_31:
	s_add_i32 s10, s10, 2
	s_lshr_b32 s4, s10, 1
	v_cvt_pk_f16_f32 v41, v40, v41
	v_cvt_pk_f16_f32 v40, v38, v39
	v_cvt_pk_f16_f32 v37, v36, v37
	v_cvt_pk_f16_f32 v36, v34, v35
	v_add_u32_e32 v34, 0x4800, v58
	s_add_i32 s5, s4, s15
	s_lshl_b32 s2, s10, 4
	ds_write2_b64 v34, v[40:41], v[36:37] offset0:96 offset1:104
	v_and_or_b32 v36, s2, 16, v102
	s_cmp_lt_u32 s5, 32
	s_cselect_b64 s[8:9], -1, 0
	s_cmp_lt_u32 s5, 16
	v_lshlrev_b32_e32 v34, 3, v36
	v_mov_b32_e32 v35, 0
	s_cselect_b64 s[2:3], -1, 0
	s_cmp_gt_u32 s5, 31
	v_lshl_add_u64 v[34:35], s[6:7], 0, v[34:35]
	s_cbranch_scc1 .LBB2_33
	v_lshlrev_b64 v[38:39], 8, v[98:99]
	v_lshl_add_u64 v[46:47], v[34:35], 0, v[38:39]
	global_load_dwordx4 v[38:41], v[46:47], off
	global_load_dwordx4 v[42:45], v[46:47], off offset:16
	s_mov_b32 s6, 0x3e38aa3b
	s_waitcnt vmcnt(0)
	v_mov_b32_e32 v47, v40
	v_mov_b32_e32 v40, v39
	v_mov_b32_e32 v39, v44
	v_mov_b32_e32 v44, v43
	v_mov_b32_e32 v46, v38
	v_mov_b32_e32 v38, v42
	v_pk_mul_f32 v[42:43], v[30:31], v[40:41]
	v_pk_mul_f32 v[40:41], v[26:27], v[40:41]
	v_pk_mul_f32 v[48:49], v[32:33], v[44:45]
	v_pk_mul_f32 v[44:45], v[28:29], v[44:45]
	v_pk_fma_f32 v[26:27], v[26:27], v[46:47], v[42:43]
	v_pk_fma_f32 v[30:31], v[30:31], v[46:47], v[40:41] neg_lo:[0,0,1] neg_hi:[0,0,1]
	v_pk_fma_f32 v[28:29], v[28:29], v[38:39], v[48:49]
	v_pk_fma_f32 v[32:33], v[32:33], v[38:39], v[44:45] neg_lo:[0,0,1] neg_hi:[0,0,1]
	s_cmp_lg_u64 s[2:3], 0
	s_cbranch_scc0 .Lqs_skip_8
	v_pk_mul_f32 v[30:31], v[30:31], s[6:7] op_sel_hi:[1,0]
	v_pk_mul_f32 v[32:33], v[32:33], s[6:7] op_sel_hi:[1,0]
	v_pk_mul_f32 v[26:27], v[26:27], s[6:7] op_sel_hi:[1,0]
	v_pk_mul_f32 v[28:29], v[28:29], s[6:7] op_sel_hi:[1,0]
.Lqs_skip_8:
.LBB2_33:
	s_lshl_b32 s4, s4, 7
	s_add_i32 s4, s4, 0
	v_lshl_add_u32 v36, v36, 1, s4
	v_cvt_pk_f16_f32 v29, v28, v29
	v_cvt_pk_f16_f32 v28, v26, v27
	v_cndmask_b32_e64 v26, 0, 1, s[8:9]
	v_cvt_pk_f16_f32 v33, v32, v33
	v_cvt_pk_f16_f32 v32, v30, v31
	v_add_u32_e32 v1, v36, v1
	v_cmp_ne_u32_e64 s[4:5], 1, v26
	s_andn2_b64 vcc, exec, s[8:9]
	ds_write2_b64 v1, v[32:33], v[28:29] offset1:8
	s_cbranch_vccnz .LBB2_35
	v_lshlrev_b64 v[26:27], 8, v[90:91]
	v_lshl_add_u64 v[36:37], v[34:35], 0, v[26:27]
	global_load_dwordx4 v[26:29], v[36:37], off
	global_load_dwordx4 v[30:33], v[36:37], off offset:16
	s_mov_b32 s6, 0x3e38aa3b
	s_waitcnt vmcnt(0)
	v_mov_b32_e32 v37, v28
	v_mov_b32_e32 v28, v27
	v_mov_b32_e32 v27, v32
	v_mov_b32_e32 v32, v31
	v_mov_b32_e32 v36, v26
	v_mov_b32_e32 v26, v30
	v_pk_mul_f32 v[30:31], v[22:23], v[28:29]
	v_pk_mul_f32 v[28:29], v[18:19], v[28:29]
	v_pk_mul_f32 v[38:39], v[24:25], v[32:33]
	v_pk_mul_f32 v[32:33], v[20:21], v[32:33]
	v_pk_fma_f32 v[18:19], v[18:19], v[36:37], v[30:31]
	v_pk_fma_f32 v[22:23], v[22:23], v[36:37], v[28:29] neg_lo:[0,0,1] neg_hi:[0,0,1]
	v_pk_fma_f32 v[20:21], v[20:21], v[26:27], v[38:39]
	v_pk_fma_f32 v[24:25], v[24:25], v[26:27], v[32:33] neg_lo:[0,0,1] neg_hi:[0,0,1]
	s_cmp_lg_u64 s[2:3], 0
	s_cbranch_scc0 .Lqs_skip_9
	v_pk_mul_f32 v[22:23], v[22:23], s[6:7] op_sel_hi:[1,0]
	v_pk_mul_f32 v[24:25], v[24:25], s[6:7] op_sel_hi:[1,0]
	v_pk_mul_f32 v[18:19], v[18:19], s[6:7] op_sel_hi:[1,0]
	v_pk_mul_f32 v[20:21], v[20:21], s[6:7] op_sel_hi:[1,0]
.Lqs_skip_9:
.LBB2_35:
	v_cvt_pk_f16_f32 v25, v24, v25
	v_cvt_pk_f16_f32 v24, v22, v23
	v_cvt_pk_f16_f32 v21, v20, v21
	v_cvt_pk_f16_f32 v20, v18, v19
	v_add_u32_e32 v18, 0x1800, v1
	s_and_b64 vcc, exec, s[4:5]
	ds_write2_b64 v18, v[24:25], v[20:21] offset0:32 offset1:40
	s_cbranch_vccnz .LBB2_37
	v_lshlrev_b64 v[18:19], 8, v[82:83]
	v_lshl_add_u64 v[26:27], v[34:35], 0, v[18:19]
	global_load_dwordx4 v[18:21], v[26:27], off
	global_load_dwordx4 v[22:25], v[26:27], off offset:16
	s_mov_b32 s6, 0x3e38aa3b
	s_waitcnt vmcnt(0)
	v_mov_b32_e32 v27, v20
	v_mov_b32_e32 v20, v19
	v_mov_b32_e32 v19, v24
	v_mov_b32_e32 v24, v23
	v_mov_b32_e32 v26, v18
	v_mov_b32_e32 v18, v22
	v_pk_mul_f32 v[22:23], v[14:15], v[20:21]
	v_pk_mul_f32 v[20:21], v[10:11], v[20:21]
	v_pk_mul_f32 v[28:29], v[16:17], v[24:25]
	v_pk_mul_f32 v[24:25], v[12:13], v[24:25]
	v_pk_fma_f32 v[10:11], v[10:11], v[26:27], v[22:23]
	v_pk_fma_f32 v[14:15], v[14:15], v[26:27], v[20:21] neg_lo:[0,0,1] neg_hi:[0,0,1]
	v_pk_fma_f32 v[12:13], v[12:13], v[18:19], v[28:29]
	v_pk_fma_f32 v[16:17], v[16:17], v[18:19], v[24:25] neg_lo:[0,0,1] neg_hi:[0,0,1]
	s_cmp_lg_u64 s[2:3], 0
	s_cbranch_scc0 .Lqs_skip_10
	v_pk_mul_f32 v[14:15], v[14:15], s[6:7] op_sel_hi:[1,0]
	v_pk_mul_f32 v[16:17], v[16:17], s[6:7] op_sel_hi:[1,0]
	v_pk_mul_f32 v[10:11], v[10:11], s[6:7] op_sel_hi:[1,0]
	v_pk_mul_f32 v[12:13], v[12:13], s[6:7] op_sel_hi:[1,0]
.Lqs_skip_10:
.LBB2_37:
	v_cvt_pk_f16_f32 v17, v16, v17
	v_cvt_pk_f16_f32 v16, v14, v15
	v_cvt_pk_f16_f32 v13, v12, v13
	v_cvt_pk_f16_f32 v12, v10, v11
	v_add_u32_e32 v10, 0x3000, v1
	s_and_b64 vcc, exec, s[4:5]
	ds_write2_b64 v10, v[16:17], v[12:13] offset0:64 offset1:72
	s_cbranch_vccnz .LBB2_39
	v_lshlrev_b64 v[10:11], 8, v[74:75]
	v_lshl_add_u64 v[18:19], v[34:35], 0, v[10:11]
	global_load_dwordx4 v[10:13], v[18:19], off
	global_load_dwordx4 v[14:17], v[18:19], off offset:16
	s_mov_b32 s4, 0x3e38aa3b
	s_waitcnt vmcnt(0)
	v_mov_b32_e32 v19, v12
	v_mov_b32_e32 v12, v11
	v_mov_b32_e32 v11, v16
	v_mov_b32_e32 v16, v15
	v_mov_b32_e32 v18, v10
	v_mov_b32_e32 v10, v14
	v_pk_mul_f32 v[14:15], v[6:7], v[12:13]
	v_pk_mul_f32 v[12:13], v[2:3], v[12:13]
	v_pk_mul_f32 v[20:21], v[8:9], v[16:17]
	v_pk_mul_f32 v[16:17], v[4:5], v[16:17]
	v_pk_fma_f32 v[2:3], v[2:3], v[18:19], v[14:15]
	v_pk_fma_f32 v[6:7], v[6:7], v[18:19], v[12:13] neg_lo:[0,0,1] neg_hi:[0,0,1]
	v_pk_fma_f32 v[4:5], v[4:5], v[10:11], v[20:21]
	v_pk_fma_f32 v[8:9], v[8:9], v[10:11], v[16:17] neg_lo:[0,0,1] neg_hi:[0,0,1]
	s_cmp_lg_u64 s[2:3], 0
	s_cbranch_scc0 .Lqs_skip_11
	v_pk_mul_f32 v[6:7], v[6:7], s[4:5] op_sel_hi:[1,0]
	v_pk_mul_f32 v[8:9], v[8:9], s[4:5] op_sel_hi:[1,0]
	v_pk_mul_f32 v[2:3], v[2:3], s[4:5] op_sel_hi:[1,0]
	v_pk_mul_f32 v[4:5], v[4:5], s[4:5] op_sel_hi:[1,0]
.Lqs_skip_11:
.LBB2_39:
	v_cvt_pk_f16_f32 v9, v8, v9
	v_cvt_pk_f16_f32 v8, v6, v7
	v_cvt_pk_f16_f32 v5, v4, v5
	v_cvt_pk_f16_f32 v4, v2, v3
	v_add_u32_e32 v1, 0x4800, v1
	s_mov_b32 s2, 0xaaaaaab
	s_load_dwordx4 s[4:7], s[0:1], 0x18
	s_load_dwordx2 s[8:9], s[0:1], 0x28
	ds_write2_b64 v1, v[8:9], v[4:5] offset0:96 offset1:104
	v_mul_hi_u32 v9, v0, s2
	v_mul_u32_u24_e32 v1, 24, v9
	v_sub_u32_e32 v10, v0, v1
	v_lshl_add_u32 v16, v10, 3, s13
	s_movk_i32 s0, 0x400
	v_and_b32_e32 v2, 0x7ffffc00, v16
	s_waitcnt lgkmcnt(0)
	v_mov_b32_e32 v1, s8
	v_mov_b32_e32 v4, s6
	v_cmp_eq_u32_e32 vcc, s0, v2
	v_mov_b32_e32 v5, s9
	v_mov_b32_e32 v6, s7
	v_cndmask_b32_e32 v2, v1, v4, vcc
	v_cndmask_b32_e32 v3, v5, v6, vcc
	v_mov_b32_e32 v7, s5
	v_cmp_gt_u32_e32 vcc, s0, v16
	v_mov_b32_e32 v8, s4
	v_or_b32_e32 v11, s12, v9
	v_cndmask_b32_e32 v3, v3, v7, vcc
	v_cndmask_b32_e32 v2, v2, v8, vcc
	s_movk_i32 s1, 0x880
	v_mad_i64_i32 v[14:15], s[4:5], v11, s1, v[2:3]
	v_mul_u32_u24_e32 v2, 0x190, v9
	v_lshlrev_b32_e32 v3, 4, v10
	s_waitcnt lgkmcnt(0)
	s_barrier
	v_add3_u32 v2, 0, v2, v3
	ds_read_b128 v[10:13], v2
	v_and_b32_e32 v2, 0x3f8, v16
	v_lshlrev_b32_e32 v2, 1, v2
	v_mov_b32_e32 v3, 0
	v_lshl_add_u64 v[14:15], v[14:15], 0, v[2:3]
	v_add_u32_e32 v2, 0x200, v0
	v_mul_hi_u32 v9, v2, s2
	s_waitcnt lgkmcnt(0)
	global_store_dwordx4 v[14:15], v[10:13], off sc1
	s_nop 1
	v_mul_u32_u24_e32 v10, 24, v9
	v_sub_u32_e32 v2, v2, v10
	v_lshl_add_u32 v16, v2, 3, s13
	v_and_b32_e32 v10, 0x7ffffc00, v16
	v_cmp_eq_u32_e32 vcc, s0, v10
	v_or_b32_e32 v17, s12, v9
	v_mul_u32_u24_e32 v9, 0x190, v9
	v_lshlrev_b32_e32 v2, 4, v2
	v_cndmask_b32_e32 v10, v1, v4, vcc
	v_cndmask_b32_e32 v11, v5, v6, vcc
	v_cmp_gt_u32_e32 vcc, s0, v16
	v_add3_u32 v2, 0, v9, v2
	s_nop 0
	v_cndmask_b32_e32 v15, v11, v7, vcc
	v_cndmask_b32_e32 v14, v10, v8, vcc
	ds_read_b128 v[10:13], v2
	v_and_b32_e32 v2, 0x3f8, v16
	v_mad_i64_i32 v[14:15], s[4:5], v17, s1, v[14:15]
	v_lshlrev_b32_e32 v2, 1, v2
	v_lshl_add_u64 v[14:15], v[14:15], 0, v[2:3]
	v_or_b32_e32 v2, 0x400, v0
	v_mul_hi_u32 v9, v2, s2
	s_waitcnt lgkmcnt(0)
	global_store_dwordx4 v[14:15], v[10:13], off sc1
	s_nop 1
	v_mul_u32_u24_e32 v10, 24, v9
	v_sub_u32_e32 v2, v2, v10
	v_lshl_add_u32 v16, v2, 3, s13
	v_and_b32_e32 v10, 0x7ffffc00, v16
	v_cmp_eq_u32_e32 vcc, s0, v10
	v_or_b32_e32 v17, s12, v9
	v_mul_u32_u24_e32 v9, 0x190, v9
	v_lshlrev_b32_e32 v2, 4, v2
	v_cndmask_b32_e32 v10, v1, v4, vcc
	v_cndmask_b32_e32 v11, v5, v6, vcc
	v_cmp_gt_u32_e32 vcc, s0, v16
	v_add3_u32 v2, 0, v9, v2
	s_nop 0
	v_cndmask_b32_e32 v15, v11, v7, vcc
	v_cndmask_b32_e32 v14, v10, v8, vcc
	ds_read_b128 v[10:13], v2
	v_and_b32_e32 v2, 0x3f8, v16
	v_mad_i64_i32 v[14:15], s[4:5], v17, s1, v[14:15]
	v_lshlrev_b32_e32 v2, 1, v2
	v_lshl_add_u64 v[14:15], v[14:15], 0, v[2:3]
	v_add_u32_e32 v2, 0x600, v0
	v_mul_hi_u32 v9, v2, s2
	s_waitcnt lgkmcnt(0)
	global_store_dwordx4 v[14:15], v[10:13], off sc1
	s_nop 1
	v_mul_u32_u24_e32 v10, 24, v9
	v_sub_u32_e32 v2, v2, v10
	v_lshl_add_u32 v16, v2, 3, s13
	v_and_b32_e32 v10, 0x7ffffc00, v16
	v_cmp_eq_u32_e32 vcc, s0, v10
	v_or_b32_e32 v17, s12, v9
	v_mul_u32_u24_e32 v9, 0x190, v9
	v_lshlrev_b32_e32 v2, 4, v2
	v_cndmask_b32_e32 v10, v1, v4, vcc
	v_cndmask_b32_e32 v11, v5, v6, vcc
	v_cmp_gt_u32_e32 vcc, s0, v16
	v_add3_u32 v2, 0, v9, v2
	s_nop 0
	v_cndmask_b32_e32 v15, v11, v7, vcc
	v_cndmask_b32_e32 v14, v10, v8, vcc
	ds_read_b128 v[10:13], v2
	v_and_b32_e32 v2, 0x3f8, v16
	v_mad_i64_i32 v[14:15], s[4:5], v17, s1, v[14:15]
	v_lshlrev_b32_e32 v2, 1, v2
	v_lshl_add_u64 v[14:15], v[14:15], 0, v[2:3]
	v_or_b32_e32 v2, 0x800, v0
	v_mul_hi_u32 v9, v2, s2
	s_waitcnt lgkmcnt(0)
	global_store_dwordx4 v[14:15], v[10:13], off sc1
	s_nop 1
	v_mul_u32_u24_e32 v10, 24, v9
	v_sub_u32_e32 v2, v2, v10
	v_lshl_add_u32 v16, v2, 3, s13
	v_and_b32_e32 v10, 0x7ffffc00, v16
	v_cmp_eq_u32_e32 vcc, s0, v10
	v_or_b32_e32 v17, s12, v9
	v_mul_u32_u24_e32 v9, 0x190, v9
	v_lshlrev_b32_e32 v2, 4, v2
	v_cndmask_b32_e32 v10, v1, v4, vcc
	v_cndmask_b32_e32 v11, v5, v6, vcc
	v_cmp_gt_u32_e32 vcc, s0, v16
	v_add3_u32 v2, 0, v9, v2
	s_nop 0
	v_cndmask_b32_e32 v15, v11, v7, vcc
	v_cndmask_b32_e32 v14, v10, v8, vcc
	ds_read_b128 v[10:13], v2
	v_and_b32_e32 v2, 0x3f8, v16
	v_mad_i64_i32 v[14:15], s[4:5], v17, s1, v[14:15]
	v_lshlrev_b32_e32 v2, 1, v2
	v_lshl_add_u64 v[14:15], v[14:15], 0, v[2:3]
	v_add_u32_e32 v2, 0xa00, v0
	v_mul_hi_u32 v9, v2, s2
	s_waitcnt lgkmcnt(0)
	global_store_dwordx4 v[14:15], v[10:13], off sc1
	s_nop 1
	v_mul_u32_u24_e32 v10, 24, v9
	v_sub_u32_e32 v2, v2, v10
	v_lshl_add_u32 v16, v2, 3, s13
	v_and_b32_e32 v10, 0x7ffffc00, v16
	v_cmp_eq_u32_e32 vcc, s0, v10
	v_or_b32_e32 v17, s12, v9
	v_mul_u32_u24_e32 v9, 0x190, v9
	v_lshlrev_b32_e32 v2, 4, v2
	v_cndmask_b32_e32 v10, v1, v4, vcc
	v_cndmask_b32_e32 v11, v5, v6, vcc
	v_cmp_gt_u32_e32 vcc, s0, v16
	v_add3_u32 v2, 0, v9, v2
	s_nop 0
	v_cndmask_b32_e32 v15, v11, v7, vcc
	v_cndmask_b32_e32 v14, v10, v8, vcc
	ds_read_b128 v[10:13], v2
	v_and_b32_e32 v2, 0x3f8, v16
	v_mad_i64_i32 v[14:15], s[4:5], v17, s1, v[14:15]
	v_lshlrev_b32_e32 v2, 1, v2
	v_lshl_add_u64 v[14:15], v[14:15], 0, v[2:3]
	v_or_b32_e32 v2, 0xc00, v0
	v_mul_hi_u32 v9, v2, s2
	s_waitcnt lgkmcnt(0)
	global_store_dwordx4 v[14:15], v[10:13], off sc1
	s_nop 1
	v_mul_u32_u24_e32 v10, 24, v9
	v_sub_u32_e32 v2, v2, v10
	v_lshl_add_u32 v16, v2, 3, s13
	v_and_b32_e32 v10, 0x7ffffc00, v16
	v_cmp_eq_u32_e32 vcc, s0, v10
	v_or_b32_e32 v17, s12, v9
	v_mul_u32_u24_e32 v9, 0x190, v9
	v_lshlrev_b32_e32 v2, 4, v2
	v_cndmask_b32_e32 v10, v1, v4, vcc
	v_cndmask_b32_e32 v11, v5, v6, vcc
	v_cmp_gt_u32_e32 vcc, s0, v16
	v_add3_u32 v2, 0, v9, v2
	s_nop 0
	v_cndmask_b32_e32 v15, v11, v7, vcc
	v_cndmask_b32_e32 v14, v10, v8, vcc
	ds_read_b128 v[10:13], v2
	v_and_b32_e32 v2, 0x3f8, v16
	v_mad_i64_i32 v[14:15], s[4:5], v17, s1, v[14:15]
	v_lshlrev_b32_e32 v2, 1, v2
	v_lshl_add_u64 v[14:15], v[14:15], 0, v[2:3]
	v_add_u32_e32 v2, 0xe00, v0
	v_mul_hi_u32 v9, v2, s2
	s_waitcnt lgkmcnt(0)
	global_store_dwordx4 v[14:15], v[10:13], off sc1
	s_nop 1
	v_mul_u32_u24_e32 v10, 24, v9
	v_sub_u32_e32 v2, v2, v10
	v_lshl_add_u32 v16, v2, 3, s13
	v_and_b32_e32 v10, 0x7ffffc00, v16
	v_cmp_eq_u32_e32 vcc, s0, v10
	v_add_u32_e32 v17, s12, v9
	v_mul_u32_u24_e32 v9, 0x190, v9
	v_lshlrev_b32_e32 v2, 4, v2
	v_cndmask_b32_e32 v10, v1, v4, vcc
	v_cndmask_b32_e32 v11, v5, v6, vcc
	v_cmp_gt_u32_e32 vcc, s0, v16
	v_add3_u32 v2, 0, v9, v2
	s_nop 0
	v_cndmask_b32_e32 v15, v11, v7, vcc
	v_cndmask_b32_e32 v14, v10, v8, vcc
	ds_read_b128 v[10:13], v2
	v_and_b32_e32 v2, 0x3f8, v16
	v_mad_i64_i32 v[14:15], s[4:5], v17, s1, v[14:15]
	v_lshlrev_b32_e32 v2, 1, v2
	v_lshl_add_u64 v[14:15], v[14:15], 0, v[2:3]
	v_or_b32_e32 v2, 0x1000, v0
	v_mul_hi_u32 v9, v2, s2
	s_waitcnt lgkmcnt(0)
	global_store_dwordx4 v[14:15], v[10:13], off sc1
	s_nop 1
	v_mul_u32_u24_e32 v10, 24, v9
	v_sub_u32_e32 v2, v2, v10
	v_lshl_add_u32 v16, v2, 3, s13
	v_and_b32_e32 v10, 0x7ffffc00, v16
	v_cmp_eq_u32_e32 vcc, s0, v10
	v_or_b32_e32 v17, s12, v9
	v_mul_u32_u24_e32 v9, 0x190, v9
	v_lshlrev_b32_e32 v2, 4, v2
	v_cndmask_b32_e32 v10, v1, v4, vcc
	v_cndmask_b32_e32 v11, v5, v6, vcc
	v_cmp_gt_u32_e32 vcc, s0, v16
	v_add3_u32 v2, 0, v9, v2
	s_nop 0
	v_cndmask_b32_e32 v15, v11, v7, vcc
	v_cndmask_b32_e32 v14, v10, v8, vcc
	ds_read_b128 v[10:13], v2
	v_and_b32_e32 v2, 0x3f8, v16
	v_mad_i64_i32 v[14:15], s[4:5], v17, s1, v[14:15]
	v_lshlrev_b32_e32 v2, 1, v2
	v_lshl_add_u64 v[14:15], v[14:15], 0, v[2:3]
	v_add_u32_e32 v2, 0x1200, v0
	v_mul_hi_u32 v9, v2, s2
	s_waitcnt lgkmcnt(0)
	global_store_dwordx4 v[14:15], v[10:13], off sc1
	s_nop 1
	v_mul_u32_u24_e32 v10, 24, v9
	v_sub_u32_e32 v2, v2, v10
	v_lshl_add_u32 v16, v2, 3, s13
	v_and_b32_e32 v10, 0x7ffffc00, v16
	v_cmp_eq_u32_e32 vcc, s0, v10
	v_or_b32_e32 v17, s12, v9
	v_mul_u32_u24_e32 v9, 0x190, v9
	v_lshlrev_b32_e32 v2, 4, v2
	v_cndmask_b32_e32 v10, v1, v4, vcc
	v_cndmask_b32_e32 v11, v5, v6, vcc
	v_cmp_gt_u32_e32 vcc, s0, v16
	v_add3_u32 v2, 0, v9, v2
	s_nop 0
	v_cndmask_b32_e32 v15, v11, v7, vcc
	v_cndmask_b32_e32 v14, v10, v8, vcc
	ds_read_b128 v[10:13], v2
	v_and_b32_e32 v2, 0x3f8, v16
	v_mad_i64_i32 v[14:15], s[4:5], v17, s1, v[14:15]
	v_lshlrev_b32_e32 v2, 1, v2
	v_lshl_add_u64 v[14:15], v[14:15], 0, v[2:3]
	v_or_b32_e32 v2, 0x1400, v0
	v_mul_hi_u32 v9, v2, s2
	s_waitcnt lgkmcnt(0)
	global_store_dwordx4 v[14:15], v[10:13], off sc1
	s_nop 1
	v_mul_u32_u24_e32 v10, 24, v9
	v_sub_u32_e32 v2, v2, v10
	v_lshl_add_u32 v16, v2, 3, s13
	v_and_b32_e32 v10, 0x7ffffc00, v16
	v_cmp_eq_u32_e32 vcc, s0, v10
	v_or_b32_e32 v17, s12, v9
	v_mul_u32_u24_e32 v9, 0x190, v9
	v_lshlrev_b32_e32 v2, 4, v2
	v_cndmask_b32_e32 v10, v1, v4, vcc
	v_cndmask_b32_e32 v11, v5, v6, vcc
	v_cmp_gt_u32_e32 vcc, s0, v16
	v_add3_u32 v2, 0, v9, v2
	v_add_u32_e32 v0, 0x1600, v0
	v_cndmask_b32_e32 v15, v11, v7, vcc
	v_cndmask_b32_e32 v14, v10, v8, vcc
	ds_read_b128 v[10:13], v2
	v_and_b32_e32 v2, 0x3f8, v16
	v_mad_i64_i32 v[14:15], s[4:5], v17, s1, v[14:15]
	v_lshlrev_b32_e32 v2, 1, v2
	v_lshl_add_u64 v[14:15], v[14:15], 0, v[2:3]
	v_mul_hi_u32 v2, v0, s2
	v_mul_u32_u24_e32 v9, 24, v2
	v_sub_u32_e32 v9, v0, v9
	s_waitcnt lgkmcnt(0)
	global_store_dwordx4 v[14:15], v[10:13], off sc1
	s_nop 1
	v_lshl_add_u32 v10, v9, 3, s13
	v_and_b32_e32 v0, 0x7ffffc00, v10
	v_cmp_eq_u32_e32 vcc, s0, v0
	s_nop 1
	v_cndmask_b32_e32 v0, v1, v4, vcc
	v_cndmask_b32_e32 v1, v5, v6, vcc
	v_cmp_gt_u32_e32 vcc, s0, v10
	v_lshlrev_b32_e32 v4, 4, v9
	s_nop 0
	v_cndmask_b32_e32 v0, v0, v8, vcc
	v_add_u32_e32 v8, s12, v2
	v_mul_u32_u24_e32 v2, 0x190, v2
	v_add3_u32 v2, 0, v2, v4
	v_cndmask_b32_e32 v1, v1, v7, vcc
	ds_read_b128 v[4:7], v2
	v_and_b32_e32 v2, 0x3f8, v10
	v_mad_i64_i32 v[0:1], s[0:1], v8, s1, v[0:1]
	v_lshlrev_b32_e32 v2, 1, v2
	v_lshl_add_u64 v[0:1], v[0:1], 0, v[2:3]
	s_waitcnt lgkmcnt(0)
	global_store_dwordx4 v[0:1], v[4:7], off sc1
	s_nop 1
